# speedup vs baseline: 1.0808x; 1.0110x over previous
.LBB1_12:
	s_mov_b32 s0, s44
	s_add_i32 s44, s44, 1
	s_cmp_ge_u32 s44, s42
	s_cselect_b64 s[22:23], -1, 0
	s_cmp_lt_u32 s44, s42
	s_cselect_b32 s2, s44, s0
	s_waitcnt vmcnt(0)
	s_lshl_b32 s0, s2, 4
	s_mov_b32 s1, s17
	s_mov_b32 m0, s43
	ds_read_b128 v[76:79], v119 offset:32768
	ds_read_b128 v[80:83], v119 offset:36864
	ds_read_b128 v[84:87], v120 offset:32768
	ds_read_b128 v[88:91], v120 offset:36864
	ds_read_b128 v[92:95], v121
	ds_read_b128 v[96:99], v121 offset:4096
	ds_read_b128 v[128:131], v122
	ds_read_b128 v[132:135], v122 offset:4096
	ds_read_b128 v[72:75], v123
	s_waitcnt lgkmcnt(0)
	v_lshl_add_u64 v[70:71], s[0:1], 2, v[2:3]
	global_load_lds_dword v[70:71], off
	ds_read_b128 v[156:159], v115
	ds_read_b128 v[160:163], v115 offset:1024
	ds_read_b128 v[164:167], v115 offset:2048
	v_cvt_pk_bf16_f32 v136, v76, v77
	v_cvt_pk_bf16_f32 v137, v78, v79
	v_cvt_pk_bf16_f32 v138, v84, v85
	v_cvt_pk_bf16_f32 v139, v86, v87
	v_cvt_pk_bf16_f32 v140, v92, v93
	v_cvt_pk_bf16_f32 v141, v94, v95
	v_cvt_pk_bf16_f32 v142, v128, v129
	v_cvt_pk_bf16_f32 v143, v130, v131
	v_cvt_pk_bf16_f32 v144, v80, v81
	v_cvt_pk_bf16_f32 v145, v82, v83
	v_cvt_pk_bf16_f32 v146, v88, v89
	v_cvt_pk_bf16_f32 v147, v90, v91
	v_cvt_pk_bf16_f32 v128, v96, v97
	v_cvt_pk_bf16_f32 v129, v98, v99
	v_cvt_pk_bf16_f32 v130, v132, v133
	v_cvt_pk_bf16_f32 v131, v134, v135
	s_lshl_b32 s0, s2, 13
	s_cmp_lt_u32 s44, s42
	s_cselect_b32 s0, s0, 0x1e848000
	ds_read_b128 v[132:135], v115 offset:3072
	s_waitcnt lgkmcnt(3)
	v_mfma_f32_16x16x32_bf16 v[148:151], v[136:139], v[156:159], v[36:39]
	ds_read_b128 v[156:159], v115 offset:4096
	s_waitcnt lgkmcnt(3)
	v_mfma_f32_16x16x32_bf16 v[152:155], v[136:139], v[160:163], v[40:43]
	ds_read_b128 v[160:163], v115 offset:5120
	s_waitcnt lgkmcnt(3)
	v_mfma_f32_16x16x32_bf16 v[96:99], v[136:139], v[164:167], v[44:47]
	ds_read_b128 v[164:167], v115 offset:6144
	s_waitcnt lgkmcnt(3)
	v_mfma_f32_16x16x32_bf16 v[92:95], v[136:139], v[132:135], v[48:51]
	s_mov_b32 m0, s47
	s_nop 0
	buffer_load_dwordx4 v113, s[12:15], s0 offen nt lds
	ds_read_b128 v[132:135], v115 offset:7168
	s_waitcnt lgkmcnt(3)
	v_mfma_f32_16x16x32_bf16 v[88:91], v[136:139], v[156:159], v[52:55]
	ds_read_b128 v[156:159], v115 offset:8192
	s_waitcnt lgkmcnt(3)
	v_mfma_f32_16x16x32_bf16 v[84:87], v[136:139], v[160:163], v[56:59]
	ds_read_b128 v[160:163], v115 offset:9216
	s_waitcnt lgkmcnt(3)
	v_mfma_f32_16x16x32_bf16 v[80:83], v[136:139], v[164:167], v[60:63]
	ds_read_b128 v[164:167], v115 offset:10240
	s_waitcnt lgkmcnt(3)
	v_mfma_f32_16x16x32_bf16 v[76:79], v[136:139], v[132:135], v[64:67]
	s_or_b32 s1, s0, 0x800
	s_mov_b32 m0, s48
	s_nop 0
	buffer_load_dwordx4 v113, s[12:15], s1 offen nt lds
	ds_read_b128 v[132:135], v115 offset:11264
	s_waitcnt lgkmcnt(3)
	v_mfma_f32_16x16x32_bf16 v[148:151], v[140:143], v[156:159], v[148:151]
	ds_read_b128 v[156:159], v115 offset:12288
	s_waitcnt lgkmcnt(3)
	v_mfma_f32_16x16x32_bf16 v[152:155], v[140:143], v[160:163], v[152:155]
	ds_read_b128 v[160:163], v115 offset:13312
	s_waitcnt lgkmcnt(3)
	v_mfma_f32_16x16x32_bf16 v[96:99], v[140:143], v[164:167], v[96:99]
	ds_read_b128 v[164:167], v115 offset:14336
	s_waitcnt lgkmcnt(3)
	v_mfma_f32_16x16x32_bf16 v[92:95], v[140:143], v[132:135], v[92:95]
	s_or_b32 s1, s0, 0x1000
	s_mov_b32 m0, s49
	s_nop 0
	buffer_load_dwordx4 v113, s[12:15], s1 offen nt lds
	ds_read_b128 v[132:135], v115 offset:15360
	s_waitcnt lgkmcnt(3)
	v_mfma_f32_16x16x32_bf16 v[88:91], v[140:143], v[156:159], v[88:91]
	ds_read_b128 v[156:159], v115 offset:16384
	s_waitcnt lgkmcnt(3)
	v_mfma_f32_16x16x32_bf16 v[84:87], v[140:143], v[160:163], v[84:87]
	ds_read_b128 v[160:163], v115 offset:17408
	s_waitcnt lgkmcnt(3)
	v_mfma_f32_16x16x32_bf16 v[80:83], v[140:143], v[164:167], v[80:83]
	ds_read_b128 v[164:167], v115 offset:18432
	s_waitcnt lgkmcnt(3)
	v_mfma_f32_16x16x32_bf16 v[76:79], v[140:143], v[132:135], v[76:79]
	s_or_b32 s1, s0, 0x1800
	s_mov_b32 m0, s50
	s_nop 0
	buffer_load_dwordx4 v113, s[12:15], s1 offen nt lds
	ds_read_b128 v[132:135], v115 offset:19456
	s_waitcnt lgkmcnt(3)
	v_mfma_f32_16x16x32_bf16 v[148:151], v[144:147], v[156:159], v[148:151]
	ds_read_b128 v[156:159], v115 offset:20480
	s_waitcnt lgkmcnt(3)
	v_mfma_f32_16x16x32_bf16 v[152:155], v[144:147], v[160:163], v[152:155]
	ds_read_b128 v[160:163], v115 offset:21504
	s_waitcnt lgkmcnt(3)
	v_mfma_f32_16x16x32_bf16 v[96:99], v[144:147], v[164:167], v[96:99]
	ds_read_b128 v[164:167], v115 offset:22528
	s_waitcnt lgkmcnt(3)
	v_mfma_f32_16x16x32_bf16 v[92:95], v[144:147], v[132:135], v[92:95]
	s_or_b32 s1, s0, 0x100
	s_mov_b32 m0, s51
	s_nop 0
	buffer_load_dwordx4 v113, s[12:15], s1 offen nt lds
	ds_read_b128 v[132:135], v115 offset:23552
	s_waitcnt lgkmcnt(3)
	v_mfma_f32_16x16x32_bf16 v[88:91], v[144:147], v[156:159], v[88:91]
	ds_read_b128 v[156:159], v115 offset:24576
	s_waitcnt lgkmcnt(3)
	v_mfma_f32_16x16x32_bf16 v[84:87], v[144:147], v[160:163], v[84:87]
	ds_read_b128 v[160:163], v115 offset:25600
	s_waitcnt lgkmcnt(3)
	v_mfma_f32_16x16x32_bf16 v[80:83], v[144:147], v[164:167], v[80:83]
	ds_read_b128 v[164:167], v115 offset:26624
	s_waitcnt lgkmcnt(3)
	v_mfma_f32_16x16x32_bf16 v[76:79], v[144:147], v[132:135], v[76:79]
	s_or_b32 s1, s0, 0x900
	s_mov_b32 m0, s52
	s_nop 0
	buffer_load_dwordx4 v113, s[12:15], s1 offen nt lds
	ds_read_b128 v[132:135], v115 offset:27648
	s_waitcnt lgkmcnt(3)
	v_mfma_f32_16x16x32_bf16 v[148:151], v[128:131], v[156:159], v[148:151]
	ds_read_b128 v[156:159], v115 offset:28672
	s_waitcnt lgkmcnt(3)
	v_mfma_f32_16x16x32_bf16 v[152:155], v[128:131], v[160:163], v[152:155]
	ds_read_b128 v[160:163], v115 offset:29696
	s_waitcnt lgkmcnt(3)
	v_mfma_f32_16x16x32_bf16 v[96:99], v[128:131], v[164:167], v[96:99]
	ds_read_b128 v[164:167], v115 offset:30720
	s_waitcnt lgkmcnt(3)
	v_mfma_f32_16x16x32_bf16 v[92:95], v[128:131], v[132:135], v[92:95]
	s_or_b32 s1, s0, 0x1100
	s_mov_b32 m0, s53
	s_nop 0
	buffer_load_dwordx4 v113, s[12:15], s1 offen nt lds
	ds_read_b128 v[132:135], v115 offset:31744
	s_waitcnt lgkmcnt(3)
	v_mfma_f32_16x16x32_bf16 v[88:91], v[128:131], v[156:159], v[88:91]
	s_waitcnt lgkmcnt(2)
	v_mfma_f32_16x16x32_bf16 v[84:87], v[128:131], v[160:163], v[84:87]
	s_waitcnt lgkmcnt(1)
	v_mfma_f32_16x16x32_bf16 v[80:83], v[128:131], v[164:167], v[80:83]
	s_waitcnt lgkmcnt(0)
	v_mfma_f32_16x16x32_bf16 v[76:79], v[128:131], v[132:135], v[76:79]
	s_or_b32 s1, s0, 0x1900
	s_mov_b32 m0, s54
	s_nop 0
	buffer_load_dwordx4 v113, s[12:15], s1 offen nt lds
	v_fma_f32 v70, v149, v149, 0
	v_fmac_f32_e32 v70, v153, v153
	v_fmac_f32_e32 v70, v97, v97
	v_fmac_f32_e32 v70, v93, v93
	v_fmac_f32_e32 v70, v89, v89
	v_fmac_f32_e32 v70, v85, v85
	v_fmac_f32_e32 v70, v81, v81
	v_fmac_f32_e32 v70, v77, v77
	v_fma_f32 v68, v148, v148, 0
	v_fmac_f32_e32 v68, v152, v152
	v_add_f32_dpp v70, v70, v70 quad_perm:[1,0,3,2] row_mask:0xf bank_mask:0xf bound_ctrl:1
	v_fmac_f32_e32 v68, v96, v96
	v_fmac_f32_e32 v68, v92, v92
	v_add_f32_dpp v70, v70, v70 quad_perm:[2,3,0,1] row_mask:0xf bank_mask:0xf bound_ctrl:1
	v_fmac_f32_e32 v68, v88, v88
	v_fmac_f32_e32 v68, v84, v84
	v_add_f32_dpp v70, v70, v70 row_half_mirror row_mask:0xf bank_mask:0xf bound_ctrl:1
	v_fmac_f32_e32 v68, v80, v80
	v_fmac_f32_e32 v68, v76, v76
	v_add_f32_dpp v70, v70, v70 row_mirror row_mask:0xf bank_mask:0xf bound_ctrl:1
	v_fmamk_f32 v70, v70, 0x3c000000, v124
	v_rsq_f32_e32 v127, v70
	v_fma_f32 v70, v150, v150, 0
	v_fmac_f32_e32 v70, v154, v154
	v_fmac_f32_e32 v70, v98, v98
	v_fmac_f32_e32 v70, v94, v94
	v_fmac_f32_e32 v70, v90, v90
	v_fmac_f32_e32 v70, v86, v86
	v_fmac_f32_e32 v70, v82, v82
	v_fmac_f32_e32 v70, v78, v78
	v_add_f32_dpp v68, v68, v68 quad_perm:[1,0,3,2] row_mask:0xf bank_mask:0xf bound_ctrl:1
	v_mul_f32_e32 v131, v127, v149
	v_add_f32_dpp v70, v70, v70 quad_perm:[1,0,3,2] row_mask:0xf bank_mask:0xf bound_ctrl:1
	v_add_f32_dpp v68, v68, v68 quad_perm:[2,3,0,1] row_mask:0xf bank_mask:0xf bound_ctrl:1
	v_mul_f32_e32 v81, v127, v81
	v_add_f32_dpp v70, v70, v70 quad_perm:[2,3,0,1] row_mask:0xf bank_mask:0xf bound_ctrl:1
	v_add_f32_dpp v68, v68, v68 row_half_mirror row_mask:0xf bank_mask:0xf bound_ctrl:1
	v_cmp_gt_u32_e64 s[0:1], s55, v72
	v_add_f32_dpp v70, v70, v70 row_half_mirror row_mask:0xf bank_mask:0xf bound_ctrl:1
	v_add_f32_dpp v68, v68, v68 row_mirror row_mask:0xf bank_mask:0xf bound_ctrl:1
	v_fmamk_f32 v68, v68, 0x3c000000, v124
	v_add_f32_dpp v70, v70, v70 row_mirror row_mask:0xf bank_mask:0xf bound_ctrl:1
	v_fmamk_f32 v70, v70, 0x3c000000, v124
	v_rsq_f32_e32 v130, v70
	v_fma_f32 v70, v151, v151, 0
	v_fmac_f32_e32 v70, v155, v155
	v_fmac_f32_e32 v70, v99, v99
	v_fmac_f32_e32 v70, v95, v95
	v_fmac_f32_e32 v70, v91, v91
	v_fmac_f32_e32 v70, v87, v87
	v_fmac_f32_e32 v70, v83, v83
	v_fmac_f32_e32 v70, v79, v79
	v_rsq_f32_e32 v68, v68
	v_mul_f32_e32 v98, v130, v98
	v_add_f32_dpp v70, v70, v70 quad_perm:[1,0,3,2] row_mask:0xf bank_mask:0xf bound_ctrl:1
	v_mul_f32_e32 v90, v130, v90
	v_mul_f32_e32 v111, v68, v148
	v_add_f32_dpp v110, v70, v70 quad_perm:[2,3,0,1] row_mask:0xf bank_mask:0xf bound_ctrl:1
	ds_read2_b32 v[70:71], v114 offset0:128 offset1:144
	ds_read2_b32 v[128:129], v125 offset1:16
	v_add_f32_dpp v110, v110, v110 row_half_mirror row_mask:0xf bank_mask:0xf bound_ctrl:1
	v_mul_f32_e32 v96, v68, v96
	v_mul_f32_e32 v92, v68, v92
	v_add_f32_dpp v110, v110, v110 row_mirror row_mask:0xf bank_mask:0xf bound_ctrl:1
	v_fmamk_f32 v110, v110, 0x3c000000, v124
	s_waitcnt lgkmcnt(0)
	v_fma_f32 v111, v111, v70, v128
	v_fma_f32 v131, v131, v70, v128
	v_exp_f32_e32 v111, v111
	v_exp_f32_e32 v131, v131
	v_rsq_f32_e32 v132, v110
	v_mul_f32_e32 v88, v68, v88
	v_add_f32_e32 v110, 1.0, v111
	v_add_f32_e32 v111, 1.0, v131
	v_mul_f32_e32 v131, v130, v150
	v_mul_f32_e32 v133, v132, v151
	v_fma_f32 v131, v131, v70, v128
	v_fma_f32 v70, v133, v70, v128
	v_exp_f32_e32 v131, v131
	v_exp_f32_e32 v70, v70
	v_rcp_f32_e32 v110, v110
	v_rcp_f32_e32 v111, v111
	v_add_f32_e32 v128, 1.0, v131
	v_add_f32_e32 v70, 1.0, v70
	v_rcp_f32_e32 v128, v128
	v_rcp_f32_e32 v70, v70
	v_mul_f32_e32 v131, v68, v152
	v_fma_f32 v131, v131, v71, v129
	v_cvt_pk_bf16_f32 v110, v110, v111
	v_cvt_pk_bf16_f32 v111, v128, v70
	v_mul_f32_e32 v128, v127, v153
	v_exp_f32_e32 v131, v131
	v_fma_f32 v128, v128, v71, v129
	v_exp_f32_e32 v128, v128
	v_mul_f32_e32 v99, v132, v99
	v_add_f32_e32 v70, 1.0, v131
	v_rcp_f32_e32 v133, v70
	v_add_f32_e32 v70, 1.0, v128
	v_mul_f32_e32 v131, v130, v154
	v_rcp_f32_e32 v134, v70
	v_mul_f32_e32 v70, v132, v155
	v_fma_f32 v131, v131, v71, v129
	v_fmac_f32_e32 v129, v70, v71
	v_exp_f32_e32 v135, v129
	ds_read2_b32 v[70:71], v114 offset0:160 offset1:176
	ds_read2_b32 v[128:129], v125 offset0:32 offset1:48
	v_exp_f32_e32 v131, v131
	v_mul_f32_e32 v91, v132, v91
	v_add_f32_e32 v135, 1.0, v135
	v_rcp_f32_e32 v135, v135
	s_waitcnt lgkmcnt(0)
	v_fma_f32 v96, v96, v70, v128
	v_exp_f32_e32 v136, v96
	v_mul_f32_e32 v96, v127, v97
	v_fma_f32 v96, v96, v70, v128
	v_exp_f32_e32 v97, v96
	v_fma_f32 v98, v98, v70, v128
	v_fma_f32 v70, v99, v70, v128
	v_exp_f32_e32 v98, v98
	v_exp_f32_e32 v70, v70
	v_add_f32_e32 v97, 1.0, v97
	v_cvt_pk_bf16_f32 v96, v133, v134
	v_add_f32_e32 v133, 1.0, v136
	v_rcp_f32_e32 v99, v97
	v_add_f32_e32 v97, 1.0, v98
	v_add_f32_e32 v70, 1.0, v70
	v_fma_f32 v92, v92, v71, v129
	v_rcp_f32_e32 v133, v133
	v_rcp_f32_e32 v128, v97
	v_rcp_f32_e32 v70, v70
	v_exp_f32_e32 v92, v92
	v_cvt_pk_bf16_f32 v98, v133, v99
	v_add_f32_e32 v131, 1.0, v131
	v_cvt_pk_bf16_f32 v99, v128, v70
	v_add_f32_e32 v70, 1.0, v92
	v_mul_f32_e32 v92, v127, v93
	v_fma_f32 v92, v92, v71, v129
	v_exp_f32_e32 v92, v92
	v_mul_f32_e32 v93, v130, v94
	v_fma_f32 v93, v93, v71, v129
	v_rcp_f32_e32 v131, v131
	v_exp_f32_e32 v93, v93
	v_rcp_f32_e32 v94, v70
	v_add_f32_e32 v70, 1.0, v92
	v_rcp_f32_e32 v128, v70
	v_mul_f32_e32 v70, v132, v95
	v_cvt_pk_bf16_f32 v97, v131, v135
	v_add_f32_e32 v131, 1.0, v93
	v_fmac_f32_e32 v129, v70, v71
	ds_read2_b32 v[70:71], v114 offset0:192 offset1:208
	ds_read2_b32 v[92:93], v125 offset0:64 offset1:80
	v_exp_f32_e32 v95, v129
	v_rcp_f32_e32 v129, v131
	v_mul_f32_e32 v84, v68, v84
	v_mul_f32_e32 v80, v68, v80
	s_waitcnt lgkmcnt(0)
	v_fma_f32 v88, v88, v70, v92
	v_exp_f32_e32 v131, v88
	v_mul_f32_e32 v88, v127, v89
	v_fma_f32 v88, v88, v70, v92
	v_exp_f32_e32 v89, v88
	v_fma_f32 v90, v90, v70, v92
	v_fma_f32 v70, v91, v70, v92
	v_exp_f32_e32 v90, v90
	v_exp_f32_e32 v70, v70
	v_add_f32_e32 v89, 1.0, v89
	v_cvt_pk_bf16_f32 v88, v94, v128
	v_add_f32_e32 v94, 1.0, v131
	v_rcp_f32_e32 v91, v89
	v_add_f32_e32 v89, 1.0, v90
	v_add_f32_e32 v70, 1.0, v70
	v_fma_f32 v84, v84, v71, v93
	v_rcp_f32_e32 v94, v94
	v_rcp_f32_e32 v92, v89
	v_rcp_f32_e32 v70, v70
	v_exp_f32_e32 v84, v84
	v_cvt_pk_bf16_f32 v90, v94, v91
	v_mul_f32_e32 v68, v68, v76
	v_cvt_pk_bf16_f32 v91, v92, v70
	v_add_f32_e32 v70, 1.0, v84
	v_mul_f32_e32 v84, v127, v85
	v_fma_f32 v84, v84, v71, v93
	v_mul_f32_e32 v85, v130, v86
	v_exp_f32_e32 v84, v84
	v_fma_f32 v85, v85, v71, v93
	v_exp_f32_e32 v85, v85
	v_rcp_f32_e32 v92, v70
	v_add_f32_e32 v70, 1.0, v84
	v_rcp_f32_e32 v84, v70
	v_add_f32_e32 v70, 1.0, v85
	v_mul_f32_e32 v85, v132, v87
	v_fmac_f32_e32 v93, v85, v71
	v_exp_f32_e32 v85, v93
	v_rcp_f32_e32 v93, v70
	ds_read2_b32 v[70:71], v114 offset0:224 offset1:240
	ds_read2_b32 v[86:87], v125 offset0:96 offset1:112
	v_mul_f32_e32 v76, v127, v77
	v_mul_f32_e32 v82, v130, v82
	v_mul_f32_e32 v83, v132, v83
	v_mul_f32_e32 v77, v130, v78
	s_waitcnt lgkmcnt(0)
	v_fma_f32 v76, v76, v71, v87
	v_mul_f32_e32 v78, v132, v79
	v_fma_f32 v80, v80, v70, v86
	v_fma_f32 v81, v81, v70, v86
	v_fma_f32 v82, v82, v70, v86
	v_fma_f32 v70, v83, v70, v86
	v_fma_f32 v68, v68, v71, v87
	v_exp_f32_e32 v76, v76
	v_fma_f32 v77, v77, v71, v87
	v_fmac_f32_e32 v87, v78, v71
	v_exp_f32_e32 v82, v82
	v_exp_f32_e32 v70, v70
	v_exp_f32_e32 v68, v68
	v_exp_f32_e32 v77, v77
	v_exp_f32_e32 v71, v87
	v_add_f32_e32 v76, 1.0, v76
	v_add_f32_e32 v82, 1.0, v82
	v_add_f32_e32 v70, 1.0, v70
	v_add_f32_e32 v68, 1.0, v68
	v_rcp_f32_e32 v78, v76
	v_add_f32_e32 v76, 1.0, v77
	v_add_f32_e32 v71, 1.0, v71
	v_rcp_f32_e32 v82, v82
	v_rcp_f32_e32 v70, v70
	v_rcp_f32_e32 v68, v68
	v_rcp_f32_e32 v79, v76
	v_rcp_f32_e32 v71, v71
	v_exp_f32_e32 v80, v80
	v_exp_f32_e32 v81, v81
	v_cvt_pk_bf16_f32 v77, v82, v70
	v_cvt_pk_bf16_f32 v78, v68, v78
	v_cvt_pk_bf16_f32 v79, v79, v71
	v_subrev_u32_e32 v68, s16, v72
	v_subrev_u32_e32 v70, s16, v73
	v_subrev_u32_e32 v71, s16, v74
	v_add_f32_e32 v95, 1.0, v95
	v_add_f32_e32 v85, 1.0, v85
	v_add_f32_e32 v80, 1.0, v80
	v_add_f32_e32 v81, 1.0, v81
	v_max3_u32 v68, v68, v70, v71
	v_subrev_u32_e32 v70, s16, v75
	v_rcp_f32_e32 v95, v95
	v_rcp_f32_e32 v85, v85
	v_rcp_f32_e32 v80, v80
	v_rcp_f32_e32 v81, v81
	v_max_u32_e32 v68, v68, v70
	v_cmp_gt_u32_e32 vcc, 16, v68
	s_cmp_eq_u64 vcc, -1
	s_cselect_b64 s[24:25], -1, 0
	s_cmp_lg_u64 vcc, -1
	v_cvt_pk_bf16_f32 v89, v129, v95
	v_cvt_pk_bf16_f32 v84, v92, v84
	v_cvt_pk_bf16_f32 v85, v93, v85
	v_cvt_pk_bf16_f32 v76, v80, v81
	s_cselect_b64 s[26:27], -1, 0
	v_cmp_gt_u32_e64 s[2:3], s55, v73
	v_cmp_gt_u32_e64 s[4:5], s55, v74
	v_cmp_gt_u32_e64 s[6:7], s55, v75
	s_mov_b32 s8, 0
	s_branch .LBB1_14

	.amdhsa_kernel _Z11main_kernelPKfPKiPK15HIP_vector_typeIjLj4EES0_PfS7_S2_i
		.amdhsa_group_segment_fixed_size 135936
		.amdhsa_private_segment_fixed_size 0
		.amdhsa_kernarg_size 320
		.amdhsa_user_sgpr_count 2
		.amdhsa_user_sgpr_dispatch_ptr 0
		.amdhsa_user_sgpr_queue_ptr 0
		.amdhsa_user_sgpr_kernarg_segment_ptr 1
		.amdhsa_user_sgpr_dispatch_id 0
		.amdhsa_user_sgpr_kernarg_preload_length 0
		.amdhsa_user_sgpr_kernarg_preload_offset 0
		.amdhsa_user_sgpr_private_segment_size 0
		.amdhsa_uses_dynamic_stack 0
		.amdhsa_enable_private_segment 0
		.amdhsa_system_sgpr_workgroup_id_x 1
		.amdhsa_system_sgpr_workgroup_id_y 0
		.amdhsa_system_sgpr_workgroup_id_z 0
		.amdhsa_system_sgpr_workgroup_info 0
		.amdhsa_system_vgpr_workitem_id 2
		.amdhsa_next_free_vgpr 168
		.amdhsa_next_free_sgpr 96
		.amdhsa_accum_offset 168
		.amdhsa_reserve_vcc 1
		.amdhsa_float_round_mode_32 0
		.amdhsa_float_round_mode_16_64 0
		.amdhsa_float_denorm_mode_32 3
		.amdhsa_float_denorm_mode_16_64 3
		.amdhsa_dx10_clamp 1
		.amdhsa_ieee_mode 1
		.amdhsa_fp16_overflow 0
		.amdhsa_tg_split 0
		.amdhsa_exception_fp_ieee_invalid_op 0
		.amdhsa_exception_fp_denorm_src 0
		.amdhsa_exception_fp_ieee_div_zero 0
		.amdhsa_exception_fp_ieee_overflow 0
		.amdhsa_exception_fp_ieee_underflow 0
		.amdhsa_exception_fp_ieee_inexact 0
		.amdhsa_exception_int_div_zero 0
	.end_amdhsa_kernel

amdhsa.kernels:
  - .agpr_count:     0
    .args:
      - .actual_access:  read_only
        .address_space:  global
        .offset:         0
        .size:           8
        .value_kind:     global_buffer
      - .actual_access:  read_only
        .address_space:  global
        .offset:         8
        .size:           8
        .value_kind:     global_buffer
      - .actual_access:  read_only
        .address_space:  global
        .offset:         16
        .size:           8
        .value_kind:     global_buffer
      - .actual_access:  read_only
        .address_space:  global
        .offset:         24
        .size:           8
        .value_kind:     global_buffer
      - .actual_access:  read_only
        .address_space:  global
        .offset:         32
        .size:           8
        .value_kind:     global_buffer
      - .actual_access:  read_only
        .address_space:  global
        .offset:         40
        .size:           8
        .value_kind:     global_buffer
      - .actual_access:  read_only
        .address_space:  global
        .offset:         48
        .size:           8
        .value_kind:     global_buffer
      - .actual_access:  read_only
        .address_space:  global
        .offset:         56
        .size:           8
        .value_kind:     global_buffer
      - .address_space:  global
        .offset:         64
        .size:           8
        .value_kind:     global_buffer
      - .offset:         72
        .size:           4
        .value_kind:     hidden_block_count_x
      - .offset:         76
        .size:           4
        .value_kind:     hidden_block_count_y
      - .offset:         80
        .size:           4
        .value_kind:     hidden_block_count_z
      - .offset:         84
        .size:           2
        .value_kind:     hidden_group_size_x
      - .offset:         86
        .size:           2
        .value_kind:     hidden_group_size_y
      - .offset:         88
        .size:           2
        .value_kind:     hidden_group_size_z
      - .offset:         90
        .size:           2
        .value_kind:     hidden_remainder_x
      - .offset:         92
        .size:           2
        .value_kind:     hidden_remainder_y
      - .offset:         94
        .size:           2
        .value_kind:     hidden_remainder_z
      - .offset:         112
        .size:           8
        .value_kind:     hidden_global_offset_x
      - .offset:         120
        .size:           8
        .value_kind:     hidden_global_offset_y
      - .offset:         128
        .size:           8
        .value_kind:     hidden_global_offset_z
      - .offset:         136
        .size:           2
        .value_kind:     hidden_grid_dims
    .group_segment_fixed_size: 256
    .kernarg_segment_align: 8
    .kernarg_segment_size: 328
    .language:       OpenCL C
    .language_version:
      - 2
      - 0
    .max_flat_workgroup_size: 256
    .name:           _Z11prep_kernelPKfS0_S0_S0_S0_S0_S0_PKiPc
    .private_segment_fixed_size: 0
    .sgpr_count:     58
    .sgpr_spill_count: 0
    .symbol:         _Z11prep_kernelPKfS0_S0_S0_S0_S0_S0_PKiPc.kd
    .uniform_work_group_size: 1
    .uses_dynamic_stack: false
    .vgpr_count:     37
    .vgpr_spill_count: 0
    .wavefront_size: 64
  - .agpr_count:     0
    .args:
      - .actual_access:  read_only
        .address_space:  global
        .offset:         0
        .size:           8
        .value_kind:     global_buffer
      - .address_space:  global
        .offset:         8
        .size:           8
        .value_kind:     global_buffer
      - .actual_access:  read_only
        .address_space:  global
        .offset:         16
        .size:           8
        .value_kind:     global_buffer
      - .actual_access:  read_only
        .address_space:  global
        .offset:         24
        .size:           8
        .value_kind:     global_buffer
      - .address_space:  global
        .offset:         32
        .size:           8
        .value_kind:     global_buffer
      - .address_space:  global
        .offset:         40
        .size:           8
        .value_kind:     global_buffer
      - .actual_access:  read_only
        .address_space:  global
        .offset:         48
        .size:           8
        .value_kind:     global_buffer
      - .offset:         56
        .size:           4
        .value_kind:     by_value
      - .offset:         64
        .size:           4
        .value_kind:     hidden_block_count_x
      - .offset:         68
        .size:           4
        .value_kind:     hidden_block_count_y
      - .offset:         72
        .size:           4
        .value_kind:     hidden_block_count_z
      - .offset:         76
        .size:           2
        .value_kind:     hidden_group_size_x
      - .offset:         78
        .size:           2
        .value_kind:     hidden_group_size_y
      - .offset:         80
        .size:           2
        .value_kind:     hidden_group_size_z
      - .offset:         82
        .size:           2
        .value_kind:     hidden_remainder_x
      - .offset:         84
        .size:           2
        .value_kind:     hidden_remainder_y
      - .offset:         86
        .size:           2
        .value_kind:     hidden_remainder_z
      - .offset:         104
        .size:           8
        .value_kind:     hidden_global_offset_x
      - .offset:         112
        .size:           8
        .value_kind:     hidden_global_offset_y
      - .offset:         120
        .size:           8
        .value_kind:     hidden_global_offset_z
      - .offset:         128
        .size:           2
        .value_kind:     hidden_grid_dims
    .group_segment_fixed_size: 135936
    .kernarg_segment_align: 8
    .kernarg_segment_size: 320
    .language:       OpenCL C
    .language_version:
      - 2
      - 0
    .max_flat_workgroup_size: 768
    .name:           _Z11main_kernelPKfPKiPK15HIP_vector_typeIjLj4EES0_PfS7_S2_i
    .private_segment_fixed_size: 0
    .sgpr_count:     66
    .sgpr_spill_count: 0
    .symbol:         _Z11main_kernelPKfPKiPK15HIP_vector_typeIjLj4EES0_PfS7_S2_i.kd
    .uniform_work_group_size: 1
    .uses_dynamic_stack: false
    .vgpr_count:     168
    .vgpr_spill_count: 0
    .wavefront_size: 64
  - .agpr_count:     60
    .args:
      - .actual_access:  read_only
        .address_space:  global
        .offset:         0
        .size:           8
        .value_kind:     global_buffer
      - .actual_access:  read_only
        .address_space:  global
        .offset:         8
        .size:           8
        .value_kind:     global_buffer
      - .actual_access:  read_only
        .address_space:  global
        .offset:         16
        .size:           8
        .value_kind:     global_buffer
      - .actual_access:  read_only
        .address_space:  global
        .offset:         24
        .size:           8
        .value_kind:     global_buffer
      - .actual_access:  read_only
        .address_space:  global
        .offset:         32
        .size:           8
        .value_kind:     global_buffer
      - .actual_access:  read_only
        .address_space:  global
        .offset:         40
        .size:           8
        .value_kind:     global_buffer
      - .actual_access:  read_only
        .address_space:  global
        .offset:         48
        .size:           8
        .value_kind:     global_buffer
      - .actual_access:  read_only
        .address_space:  global
        .offset:         56
        .size:           8
        .value_kind:     global_buffer
      - .address_space:  global
        .offset:         64
        .size:           8
        .value_kind:     global_buffer
    .group_segment_fixed_size: 86272
    .kernarg_segment_align: 8
    .kernarg_segment_size: 72
    .language:       OpenCL C
    .language_version:
      - 2
      - 0
    .max_flat_workgroup_size: 256
    .name:           _Z10enc_kernelPKfS0_PK15HIP_vector_typeIjLj4EES4_S4_S0_S0_S0_Pf
    .private_segment_fixed_size: 0
    .sgpr_count:     24
    .sgpr_spill_count: 0
    .symbol:         _Z10enc_kernelPKfS0_PK15HIP_vector_typeIjLj4EES4_S4_S0_S0_S0_Pf.kd
    .uniform_work_group_size: 1
    .uses_dynamic_stack: false
    .vgpr_count:     252
    .vgpr_spill_count: 0
    .wavefront_size: 64
